# same edits as before, but every hand-placed wait is now a full drain (no counted vmcnt across interleaved stores: stores retire out of order with loads); LDS waits lgkmcnt(0)
# speedup vs baseline: 1.0078x; 1.0000x over previous
.LBB0_335:
	s_lshl_b32 s2, s42, 5
	s_and_b32 s6, s42, 63
	s_and_b32 s7, s2, 0xfffff800
	s_lshl_b32 s57, s6, 4
	s_or_b32 s50, s6, s47
	s_lshl_b64 s[20:21], s[50:51], 6
	s_lshl_b64 s[2:3], s[50:51], 2
	s_add_u32 s2, s16, s2
	s_addc_u32 s3, s17, s3
	v_or_b32_e32 v2, s57, v73
	v_lshlrev_b32_e32 v0, 1, v2
	v_add_u32_e32 v2, s7, v81
	v_ashrrev_i32_e32 v3, 31, v2
	v_lshlrev_b64 v[6:7], 11, v[2:3]
	v_or_b32_e32 v6, v6, v0
	v_lshl_add_u64 v[2:3], s[30:31], 0, v[6:7]
	v_lshl_add_u64 v[6:7], s[40:41], 0, v[6:7]
	global_load_dwordx4 v[160:163], v[2:3], off
	global_load_dwordx4 v[164:167], v[6:7], off
	v_add_u32_e32 v2, s7, v83
	v_ashrrev_i32_e32 v3, 31, v2
	v_lshlrev_b64 v[6:7], 11, v[2:3]
	v_or_b32_e32 v6, v6, v0
	v_lshl_add_u64 v[2:3], s[30:31], 0, v[6:7]
	v_lshl_add_u64 v[6:7], s[40:41], 0, v[6:7]
	global_load_dwordx4 v[168:171], v[2:3], off
	global_load_dwordx4 v[172:175], v[6:7], off
	v_add_u32_e32 v2, s7, v85
	v_ashrrev_i32_e32 v3, 31, v2
	v_lshlrev_b64 v[6:7], 11, v[2:3]
	v_or_b32_e32 v6, v6, v0
	v_lshl_add_u64 v[2:3], s[30:31], 0, v[6:7]
	v_lshl_add_u64 v[6:7], s[40:41], 0, v[6:7]
	global_load_dwordx4 v[176:179], v[2:3], off
	global_load_dwordx4 v[180:183], v[6:7], off
	v_add_u32_e32 v2, s7, v104
	v_ashrrev_i32_e32 v3, 31, v2
	v_lshlrev_b64 v[6:7], 11, v[2:3]
	v_or_b32_e32 v6, v6, v0
	v_lshl_add_u64 v[2:3], s[30:31], 0, v[6:7]
	v_lshl_add_u64 v[6:7], s[40:41], 0, v[6:7]
	global_load_dwordx4 v[184:187], v[2:3], off
	global_load_dwordx4 v[188:191], v[6:7], off
	v_add_u32_e32 v2, s7, v105
	v_ashrrev_i32_e32 v3, 31, v2
	v_lshlrev_b64 v[6:7], 11, v[2:3]
	v_or_b32_e32 v6, v6, v0
	v_lshl_add_u64 v[2:3], s[30:31], 0, v[6:7]
	v_lshl_add_u64 v[6:7], s[40:41], 0, v[6:7]
	global_load_dwordx4 v[192:195], v[2:3], off
	global_load_dwordx4 v[196:199], v[6:7], off
	v_add_u32_e32 v2, s7, v106
	v_ashrrev_i32_e32 v3, 31, v2
	v_lshlrev_b64 v[6:7], 11, v[2:3]
	v_or_b32_e32 v6, v6, v0
	v_lshl_add_u64 v[2:3], s[30:31], 0, v[6:7]
	v_lshl_add_u64 v[6:7], s[40:41], 0, v[6:7]
	global_load_dwordx4 v[200:203], v[2:3], off
	global_load_dwordx4 v[204:207], v[6:7], off
	v_add_u32_e32 v2, s7, v107
	v_ashrrev_i32_e32 v3, 31, v2
	v_lshlrev_b64 v[6:7], 11, v[2:3]
	v_or_b32_e32 v6, v6, v0
	v_lshl_add_u64 v[2:3], s[30:31], 0, v[6:7]
	v_lshl_add_u64 v[6:7], s[40:41], 0, v[6:7]
	global_load_dwordx4 v[212:215], v[2:3], off
	global_load_dwordx4 v[220:223], v[6:7], off
	v_add_u32_e32 v2, s7, v108
	v_ashrrev_i32_e32 v3, 31, v2
	v_lshlrev_b64 v[6:7], 11, v[2:3]
	v_or_b32_e32 v6, v6, v0
	v_lshl_add_u64 v[2:3], s[30:31], 0, v[6:7]
	v_lshl_add_u64 v[6:7], s[40:41], 0, v[6:7]
	global_load_dwordx4 v[224:227], v[2:3], off
	global_load_dwordx4 v[244:247], v[6:7], off
	global_load_dword v158, v209, s[2:3]
	s_waitcnt vmcnt(0)
	v_lshlrev_b32_e32 v10, 16, v160
	v_and_b32_e32 v11, 0xffff0000, v160
	v_lshlrev_b32_e32 v12, 16, v164
	v_and_b32_e32 v13, 0xffff0000, v164
	v_pk_add_f32 v[10:11], v[10:11], v[12:13]
	v_lshlrev_b32_e32 v164, 16, v165
	v_cvt_pk_bf16_f32 v160, v10, v11
	v_lshlrev_b32_e32 v10, 16, v161
	v_and_b32_e32 v11, 0xffff0000, v161
	v_and_b32_e32 v165, 0xffff0000, v165
	v_pk_add_f32 v[164:165], v[10:11], v[164:165]
	v_lshlrev_b32_e32 v10, 16, v166
	v_cvt_pk_bf16_f32 v161, v164, v165
	v_lshlrev_b32_e32 v164, 16, v162
	v_and_b32_e32 v165, 0xffff0000, v162
	v_and_b32_e32 v11, 0xffff0000, v166
	v_pk_add_f32 v[164:165], v[164:165], v[10:11]
	v_lshlrev_b32_e32 v166, 16, v167
	v_cvt_pk_bf16_f32 v162, v164, v165
	v_lshlrev_b32_e32 v164, 16, v163
	v_and_b32_e32 v165, 0xffff0000, v163
	v_and_b32_e32 v167, 0xffff0000, v167
	v_pk_add_f32 v[164:165], v[164:165], v[166:167]
	s_nop 0
	v_cvt_pk_bf16_f32 v163, v164, v165
	ds_write_b128 v115, v[160:163]
	v_lshlrev_b32_e32 v10, 16, v168
	v_and_b32_e32 v11, 0xffff0000, v168
	v_lshlrev_b32_e32 v12, 16, v172
	v_and_b32_e32 v13, 0xffff0000, v172
	v_pk_add_f32 v[10:11], v[10:11], v[12:13]
	v_lshlrev_b32_e32 v172, 16, v173
	v_cvt_pk_bf16_f32 v168, v10, v11
	v_lshlrev_b32_e32 v10, 16, v169
	v_and_b32_e32 v11, 0xffff0000, v169
	v_and_b32_e32 v173, 0xffff0000, v173
	v_pk_add_f32 v[172:173], v[10:11], v[172:173]
	v_lshlrev_b32_e32 v10, 16, v174
	v_cvt_pk_bf16_f32 v169, v172, v173
	v_lshlrev_b32_e32 v172, 16, v170
	v_and_b32_e32 v173, 0xffff0000, v170
	v_and_b32_e32 v11, 0xffff0000, v174
	v_pk_add_f32 v[172:173], v[172:173], v[10:11]
	v_lshlrev_b32_e32 v174, 16, v175
	v_cvt_pk_bf16_f32 v170, v172, v173
	v_lshlrev_b32_e32 v172, 16, v171
	v_and_b32_e32 v173, 0xffff0000, v171
	v_and_b32_e32 v175, 0xffff0000, v175
	v_pk_add_f32 v[172:173], v[172:173], v[174:175]
	s_nop 0
	v_cvt_pk_bf16_f32 v171, v172, v173
	ds_write_b128 v116, v[168:171]
	v_lshlrev_b32_e32 v10, 16, v176
	v_and_b32_e32 v11, 0xffff0000, v176
	v_lshlrev_b32_e32 v12, 16, v180
	v_and_b32_e32 v13, 0xffff0000, v180
	v_pk_add_f32 v[10:11], v[10:11], v[12:13]
	v_lshlrev_b32_e32 v180, 16, v181
	v_cvt_pk_bf16_f32 v176, v10, v11
	v_lshlrev_b32_e32 v10, 16, v177
	v_and_b32_e32 v11, 0xffff0000, v177
	v_and_b32_e32 v181, 0xffff0000, v181
	v_pk_add_f32 v[180:181], v[10:11], v[180:181]
	v_lshlrev_b32_e32 v10, 16, v182
	v_cvt_pk_bf16_f32 v177, v180, v181
	v_lshlrev_b32_e32 v180, 16, v178
	v_and_b32_e32 v181, 0xffff0000, v178
	v_and_b32_e32 v11, 0xffff0000, v182
	v_pk_add_f32 v[180:181], v[180:181], v[10:11]
	v_lshlrev_b32_e32 v182, 16, v183
	v_cvt_pk_bf16_f32 v178, v180, v181
	v_lshlrev_b32_e32 v180, 16, v179
	v_and_b32_e32 v181, 0xffff0000, v179
	v_and_b32_e32 v183, 0xffff0000, v183
	v_pk_add_f32 v[180:181], v[180:181], v[182:183]
	s_nop 0
	v_cvt_pk_bf16_f32 v179, v180, v181
	ds_write_b128 v117, v[176:179]
	v_lshlrev_b32_e32 v10, 16, v184
	v_and_b32_e32 v11, 0xffff0000, v184
	v_lshlrev_b32_e32 v12, 16, v188
	v_and_b32_e32 v13, 0xffff0000, v188
	v_pk_add_f32 v[10:11], v[10:11], v[12:13]
	v_lshlrev_b32_e32 v188, 16, v189
	v_cvt_pk_bf16_f32 v184, v10, v11
	v_lshlrev_b32_e32 v10, 16, v185
	v_and_b32_e32 v11, 0xffff0000, v185
	v_and_b32_e32 v189, 0xffff0000, v189
	v_pk_add_f32 v[188:189], v[10:11], v[188:189]
	v_lshlrev_b32_e32 v10, 16, v190
	v_cvt_pk_bf16_f32 v185, v188, v189
	v_lshlrev_b32_e32 v188, 16, v186
	v_and_b32_e32 v189, 0xffff0000, v186
	v_and_b32_e32 v11, 0xffff0000, v190
	v_pk_add_f32 v[188:189], v[188:189], v[10:11]
	v_lshlrev_b32_e32 v190, 16, v191
	v_cvt_pk_bf16_f32 v186, v188, v189
	v_lshlrev_b32_e32 v188, 16, v187
	v_and_b32_e32 v189, 0xffff0000, v187
	v_and_b32_e32 v191, 0xffff0000, v191
	v_pk_add_f32 v[188:189], v[188:189], v[190:191]
	s_nop 0
	v_cvt_pk_bf16_f32 v187, v188, v189
	ds_write_b128 v118, v[184:187]
	v_lshlrev_b32_e32 v10, 16, v192
	v_and_b32_e32 v11, 0xffff0000, v192
	v_lshlrev_b32_e32 v12, 16, v196
	v_and_b32_e32 v13, 0xffff0000, v196
	v_pk_add_f32 v[10:11], v[10:11], v[12:13]
	v_lshlrev_b32_e32 v196, 16, v197
	v_cvt_pk_bf16_f32 v192, v10, v11
	v_lshlrev_b32_e32 v10, 16, v193
	v_and_b32_e32 v11, 0xffff0000, v193
	v_and_b32_e32 v197, 0xffff0000, v197
	v_pk_add_f32 v[196:197], v[10:11], v[196:197]
	v_lshlrev_b32_e32 v10, 16, v198
	v_cvt_pk_bf16_f32 v193, v196, v197
	v_lshlrev_b32_e32 v196, 16, v194
	v_and_b32_e32 v197, 0xffff0000, v194
	v_and_b32_e32 v11, 0xffff0000, v198
	v_pk_add_f32 v[196:197], v[196:197], v[10:11]
	v_lshlrev_b32_e32 v198, 16, v199
	v_cvt_pk_bf16_f32 v194, v196, v197
	v_lshlrev_b32_e32 v196, 16, v195
	v_and_b32_e32 v197, 0xffff0000, v195
	v_and_b32_e32 v199, 0xffff0000, v199
	v_pk_add_f32 v[196:197], v[196:197], v[198:199]
	s_nop 0
	v_cvt_pk_bf16_f32 v195, v196, v197
	ds_write_b128 v119, v[192:195]
	v_lshlrev_b32_e32 v10, 16, v200
	v_and_b32_e32 v11, 0xffff0000, v200
	v_lshlrev_b32_e32 v12, 16, v204
	v_and_b32_e32 v13, 0xffff0000, v204
	v_pk_add_f32 v[10:11], v[10:11], v[12:13]
	v_lshlrev_b32_e32 v204, 16, v205
	v_cvt_pk_bf16_f32 v200, v10, v11
	v_lshlrev_b32_e32 v10, 16, v201
	v_and_b32_e32 v11, 0xffff0000, v201
	v_and_b32_e32 v205, 0xffff0000, v205
	v_pk_add_f32 v[204:205], v[10:11], v[204:205]
	v_lshlrev_b32_e32 v10, 16, v206
	v_cvt_pk_bf16_f32 v201, v204, v205
	v_lshlrev_b32_e32 v204, 16, v202
	v_and_b32_e32 v205, 0xffff0000, v202
	v_and_b32_e32 v11, 0xffff0000, v206
	v_pk_add_f32 v[204:205], v[204:205], v[10:11]
	v_lshlrev_b32_e32 v206, 16, v207
	v_cvt_pk_bf16_f32 v202, v204, v205
	v_lshlrev_b32_e32 v204, 16, v203
	v_and_b32_e32 v205, 0xffff0000, v203
	v_and_b32_e32 v207, 0xffff0000, v207
	v_pk_add_f32 v[204:205], v[204:205], v[206:207]
	s_nop 0
	v_cvt_pk_bf16_f32 v203, v204, v205
	ds_write_b128 v120, v[200:203]
	v_lshlrev_b32_e32 v10, 16, v212
	v_and_b32_e32 v11, 0xffff0000, v212
	v_lshlrev_b32_e32 v12, 16, v220
	v_and_b32_e32 v13, 0xffff0000, v220
	v_pk_add_f32 v[10:11], v[10:11], v[12:13]
	v_lshlrev_b32_e32 v220, 16, v221
	v_cvt_pk_bf16_f32 v212, v10, v11
	v_lshlrev_b32_e32 v10, 16, v213
	v_and_b32_e32 v11, 0xffff0000, v213
	v_and_b32_e32 v221, 0xffff0000, v221
	v_pk_add_f32 v[220:221], v[10:11], v[220:221]
	v_lshlrev_b32_e32 v10, 16, v222
	v_cvt_pk_bf16_f32 v213, v220, v221
	v_lshlrev_b32_e32 v220, 16, v214
	v_and_b32_e32 v221, 0xffff0000, v214
	v_and_b32_e32 v11, 0xffff0000, v222
	v_pk_add_f32 v[220:221], v[220:221], v[10:11]
	v_lshlrev_b32_e32 v222, 16, v223
	v_cvt_pk_bf16_f32 v214, v220, v221
	v_lshlrev_b32_e32 v220, 16, v215
	v_and_b32_e32 v221, 0xffff0000, v215
	v_and_b32_e32 v223, 0xffff0000, v223
	v_pk_add_f32 v[220:221], v[220:221], v[222:223]
	s_nop 0
	v_cvt_pk_bf16_f32 v215, v220, v221
	ds_write_b128 v121, v[212:215]
	v_lshlrev_b32_e32 v10, 16, v224
	v_and_b32_e32 v11, 0xffff0000, v224
	v_lshlrev_b32_e32 v12, 16, v244
	v_and_b32_e32 v13, 0xffff0000, v244
	v_pk_add_f32 v[10:11], v[10:11], v[12:13]
	v_lshlrev_b32_e32 v244, 16, v245
	v_cvt_pk_bf16_f32 v224, v10, v11
	v_lshlrev_b32_e32 v10, 16, v225
	v_and_b32_e32 v11, 0xffff0000, v225
	v_and_b32_e32 v245, 0xffff0000, v245
	v_pk_add_f32 v[244:245], v[10:11], v[244:245]
	v_lshlrev_b32_e32 v10, 16, v246
	v_cvt_pk_bf16_f32 v225, v244, v245
	v_lshlrev_b32_e32 v244, 16, v226
	v_and_b32_e32 v245, 0xffff0000, v226
	v_and_b32_e32 v11, 0xffff0000, v246
	v_pk_add_f32 v[244:245], v[244:245], v[10:11]
	v_lshlrev_b32_e32 v246, 16, v247
	v_cvt_pk_bf16_f32 v226, v244, v245
	v_lshlrev_b32_e32 v244, 16, v227
	v_and_b32_e32 v245, 0xffff0000, v227
	v_and_b32_e32 v247, 0xffff0000, v247
	v_pk_add_f32 v[244:245], v[244:245], v[246:247]
	s_nop 0
	v_cvt_pk_bf16_f32 v227, v244, v245
	ds_write_b128 v122, v[224:227]
	s_waitcnt vmcnt(0)
	v_mov_b32_e32 v0, v158
	v_mul_f32_e32 v1, 0x3fb8aa3b, v0
	v_fma_f32 v2, v0, s0, -v1
	v_rndne_f32_e32 v3, v1
	v_fmac_f32_e32 v2, 0x32a5705f, v0
	v_sub_f32_e32 v1, v1, v3
	v_add_f32_e32 v1, v1, v2
	v_exp_f32_e32 v1, v1
	v_cvt_i32_f32_e32 v2, v3
	v_cmp_ngt_f32_e32 vcc, s29, v0
	v_ldexp_f32 v1, v1, v2
	s_nop 0
	v_cndmask_b32_e32 v1, 0, v1, vcc
	v_cmp_nlt_f32_e32 vcc, s92, v0
	v_or_b32_e32 v0, s20, v72
	s_nop 0
	v_cndmask_b32_e32 v68, v235, v1, vcc
	v_mov_b32_e32 v1, s21
	v_lshlrev_b64 v[0:1], 2, v[0:1]
	v_lshl_add_u64 v[2:3], s[12:13], 0, v[0:1]
	v_lshl_add_u64 v[0:1], s[14:15], 0, v[0:1]
	global_load_dword v0, v[0:1], off
	s_waitcnt vmcnt(0)
	v_mul_f32_e32 v70, v68, v0
	global_load_dword v69, v[2:3], off
	v_and_b32_e32 v71, 0x7fffffff, v70
	v_lshrrev_b32_e32 v0, 23, v71
	v_and_b32_e32 v2, 0x7fffff, v71
	v_cmp_nlt_f32_e64 s[22:23], |v70|, s77
	v_add_u32_e32 v1, 0xffffff88, v0
	v_or_b32_e32 v0, 0x800000, v2
	s_and_saveexec_b64 s[2:3], s[22:23]
	s_xor_b64 s[24:25], exec, s[2:3]
	s_cbranch_execz .LBB0_337
	v_cmp_lt_u32_e32 vcc, 63, v1
	s_nop 1
	v_cndmask_b32_e32 v2, 0, v236, vcc
	v_add_u32_e32 v2, v2, v1
	v_cmp_lt_u32_e64 s[6:7], 31, v2
	s_nop 1
	v_cndmask_b32_e64 v3, 0, v237, s[6:7]
	v_add_u32_e32 v2, v3, v2
	v_cmp_lt_u32_e64 s[8:9], 31, v2
	s_nop 1
	v_cndmask_b32_e64 v3, 0, v237, s[8:9]
	v_add_u32_e32 v16, v3, v2
	v_mad_u64_u32 v[2:3], s[2:3], v0, s85, 0
	v_mov_b32_e32 v208, v3
	v_mad_u64_u32 v[4:5], s[2:3], v0, s64, v[208:209]
	v_mov_b32_e32 v208, v5
	v_mad_u64_u32 v[6:7], s[2:3], v0, s65, v[208:209]
	v_mov_b32_e32 v208, v7
	v_mad_u64_u32 v[8:9], s[2:3], v0, s72, v[208:209]
	v_mov_b32_e32 v208, v9
	v_mad_u64_u32 v[10:11], s[2:3], v0, s73, v[208:209]
	v_mov_b32_e32 v208, v11
	v_mad_u64_u32 v[12:13], s[2:3], v0, s79, v[208:209]
	v_mov_b32_e32 v208, v13
	v_mad_u64_u32 v[14:15], s[2:3], v0, s84, v[208:209]
	v_cndmask_b32_e32 v3, v12, v8, vcc
	v_cndmask_b32_e32 v5, v14, v10, vcc
	v_cndmask_b32_e32 v9, v15, v12, vcc
	v_cndmask_b32_e64 v7, v5, v3, s[6:7]
	v_cndmask_b32_e64 v5, v9, v5, s[6:7]
	v_cndmask_b32_e32 v9, v10, v6, vcc
	v_cndmask_b32_e64 v3, v3, v9, s[6:7]
	v_cndmask_b32_e32 v4, v8, v4, vcc
	v_cndmask_b32_e64 v5, v5, v7, s[8:9]
	v_cndmask_b32_e64 v7, v7, v3, s[8:9]
	v_sub_u32_e32 v10, 32, v16
	v_cndmask_b32_e64 v8, v9, v4, s[6:7]
	v_alignbit_b32 v11, v5, v7, v10
	v_cmp_eq_u32_e64 s[10:11], 0, v16
	v_cndmask_b32_e64 v3, v3, v8, s[8:9]
	v_alignbit_b32 v9, v7, v3, v10
	v_cndmask_b32_e64 v5, v11, v5, s[10:11]
	v_cndmask_b32_e32 v2, v6, v2, vcc
	v_cndmask_b32_e64 v7, v9, v7, s[10:11]
	v_bfe_u32 v12, v5, 29, 1
	v_cndmask_b32_e64 v2, v4, v2, s[6:7]
	v_alignbit_b32 v9, v5, v7, 30
	v_sub_u32_e32 v13, 0, v12
	v_cndmask_b32_e64 v2, v8, v2, s[8:9]
	v_xor_b32_e32 v9, v9, v13
	v_alignbit_b32 v4, v3, v2, v10
	v_cndmask_b32_e64 v3, v4, v3, s[10:11]
	v_ffbh_u32_e32 v6, v9
	v_alignbit_b32 v4, v7, v3, 30
	v_min_u32_e32 v6, 32, v6
	v_alignbit_b32 v2, v3, v2, 30
	v_xor_b32_e32 v4, v4, v13
	v_sub_u32_e32 v7, 31, v6
	v_xor_b32_e32 v2, v2, v13
	v_alignbit_b32 v8, v9, v4, v7
	v_alignbit_b32 v2, v4, v2, v7
	v_alignbit_b32 v3, v8, v2, 9
	v_ffbh_u32_e32 v4, v3
	v_min_u32_e32 v4, 32, v4
	v_lshrrev_b32_e32 v11, 29, v5
	v_not_b32_e32 v7, v4
	v_alignbit_b32 v2, v3, v2, v7
	v_lshlrev_b32_e32 v3, 31, v11
	v_or_b32_e32 v7, 0x33000000, v3
	v_add_lshl_u32 v4, v4, v6, 23
	v_lshrrev_b32_e32 v2, 9, v2
	v_sub_u32_e32 v4, v7, v4
	v_or_b32_e32 v3, 0.5, v3
	v_lshlrev_b32_e32 v6, 23, v6
	v_or_b32_e32 v2, v4, v2
	v_lshrrev_b32_e32 v4, 9, v8
	v_sub_u32_e32 v3, v3, v6
	v_or_b32_e32 v3, v4, v3
	v_mul_f32_e32 v4, 0x3fc90fda, v3
	s_mov_b32 s2, 0x3fc90fda
	v_fma_f32 v6, v3, s2, -v4
	v_fmac_f32_e32 v6, 0x33a22168, v3
	v_fmac_f32_e32 v6, 0x3fc90fda, v2
	v_lshrrev_b32_e32 v2, 30, v5
	v_add_f32_e32 v96, v4, v6
	v_add_u32_e32 v95, v12, v2

.LBB0_592:
	s_or_b64 exec, exec, s[6:7]
	s_waitcnt lgkmcnt(0)
	s_barrier
	ds_read_b32 v84, v144
	ds_read_u16 v244, v164
	ds_read_u16 v245, v166
	ds_read_u16 v246, v168
	ds_read_u16 v247, v170
	ds_read_b32 v85, v146
	ds_read_b32 v91, v149
	ds_read_b32 v86, v150
	ds_read_b32 v117, v151
	ds_read_b32 v87, v152
	ds_read_b32 v119, v153
	ds_read_b32 v90, v154
	ds_read_b32 v243, v155
	v_add_u32_e32 v88, s30, v111
	v_ashrrev_i32_e32 v89, 31, v88
	v_lshlrev_b64 v[88:89], 12, v[88:89]
	s_add_i32 s26, s26, 1
	v_lshl_add_u64 v[88:89], v[126:127], 0, v[88:89]
	s_waitcnt lgkmcnt(0)
	v_lshlrev_b32_e32 v244, 16, v244
	v_lshlrev_b32_e32 v245, 16, v245
	v_lshlrev_b32_e32 v246, 16, v246
	v_lshlrev_b32_e32 v247, 16, v247
	v_mul_f32_e32 v248, 0x3d372713, v244
	v_mul_f32_e32 v249, 0x3d372713, v245
	v_mul_f32_e32 v250, 0x3d372713, v246
	v_mul_f32_e32 v251, 0x3d372713, v247
	v_mul_f32_e32 v248, v248, v244
	v_mul_f32_e32 v249, v249, v245
	v_mul_f32_e32 v250, v250, v246
	v_mul_f32_e32 v251, v251, v247
	v_fma_f32 v248, v248, v244, v244
	v_fma_f32 v249, v249, v245, v245
	v_fma_f32 v250, v250, v246, v246
	v_fma_f32 v251, v251, v247, v247
	v_mul_f32_e32 v248, 0x3fcc422a, v248
	v_mul_f32_e32 v249, 0x3fcc422a, v249
	v_mul_f32_e32 v250, 0x3fcc422a, v250
	v_mul_f32_e32 v251, 0x3fcc422a, v251
	v_mul_f32_e32 v248, 0xbfb8aa3b, v248
	v_mul_f32_e32 v249, 0xbfb8aa3b, v249
	v_mul_f32_e32 v250, 0xbfb8aa3b, v250
	v_mul_f32_e32 v251, 0xbfb8aa3b, v251
	v_exp_f32_e32 v248, v248
	v_exp_f32_e32 v249, v249
	v_exp_f32_e32 v250, v250
	v_exp_f32_e32 v251, v251
	v_add_f32_e32 v248, 1.0, v248
	v_add_f32_e32 v249, 1.0, v249
	v_add_f32_e32 v250, 1.0, v250
	v_add_f32_e32 v251, 1.0, v251
	v_rcp_f32_e32 v248, v248
	v_rcp_f32_e32 v249, v249
	v_rcp_f32_e32 v250, v250
	v_rcp_f32_e32 v251, v251
	v_mul_f32_e32 v244, v248, v244
	v_mul_f32_e32 v245, v249, v245
	v_mul_f32_e32 v246, v250, v246
	v_mul_f32_e32 v247, v251, v247
	s_waitcnt lgkmcnt(0)
	v_fmac_f32_e32 v91, v84, v85
	v_mul_f32_e32 v248, v91, v244
	v_bfe_u32 v244, v248, 16, 1
	v_add3_u32 v248, v248, v244, s82
	ds_write_b16_d16_hi v165, v248
	v_fmac_f32_e32 v117, v91, v86
	v_mul_f32_e32 v249, v117, v245
	v_bfe_u32 v245, v249, 16, 1
	v_add3_u32 v249, v249, v245, s82
	ds_write_b16_d16_hi v167, v249
	v_fmac_f32_e32 v119, v117, v87
	v_mul_f32_e32 v250, v119, v246
	v_bfe_u32 v246, v250, 16, 1
	v_add3_u32 v250, v250, v246, s82
	ds_write_b16_d16_hi v169, v250
	v_fmac_f32_e32 v243, v119, v90
	v_mul_f32_e32 v251, v243, v247
	v_bfe_u32 v247, v251, 16, 1
	v_add3_u32 v251, v251, v247, s82
	ds_write_b16_d16_hi v171, v251
	v_mov_b32_e32 v84, v243
	s_waitcnt lgkmcnt(0)
	ds_read_u16 v244, v172
	ds_read_u16 v245, v174
	ds_read_u16 v246, v176
	ds_read_u16 v247, v178
	ds_read_b32 v85, v156
	ds_read_b32 v91, v157
	ds_read_b32 v86, v158
	ds_read_b32 v117, v159
	ds_read_b32 v87, v160
	ds_read_b32 v119, v161
	ds_read_b32 v90, v162
	ds_read_b32 v243, v163
	s_waitcnt lgkmcnt(0)
	v_lshlrev_b32_e32 v244, 16, v244
	v_lshlrev_b32_e32 v245, 16, v245
	v_lshlrev_b32_e32 v246, 16, v246
	v_lshlrev_b32_e32 v247, 16, v247
	v_mul_f32_e32 v248, 0x3d372713, v244
	v_mul_f32_e32 v249, 0x3d372713, v245
	v_mul_f32_e32 v250, 0x3d372713, v246
	v_mul_f32_e32 v251, 0x3d372713, v247
	v_mul_f32_e32 v248, v248, v244
	v_mul_f32_e32 v249, v249, v245
	v_mul_f32_e32 v250, v250, v246
	v_mul_f32_e32 v251, v251, v247
	v_fma_f32 v248, v248, v244, v244
	v_fma_f32 v249, v249, v245, v245
	v_fma_f32 v250, v250, v246, v246
	v_fma_f32 v251, v251, v247, v247
	v_mul_f32_e32 v248, 0x3fcc422a, v248
	v_mul_f32_e32 v249, 0x3fcc422a, v249
	v_mul_f32_e32 v250, 0x3fcc422a, v250
	v_mul_f32_e32 v251, 0x3fcc422a, v251
	v_mul_f32_e32 v248, 0xbfb8aa3b, v248
	v_mul_f32_e32 v249, 0xbfb8aa3b, v249
	v_mul_f32_e32 v250, 0xbfb8aa3b, v250
	v_mul_f32_e32 v251, 0xbfb8aa3b, v251
	v_exp_f32_e32 v248, v248
	v_exp_f32_e32 v249, v249
	v_exp_f32_e32 v250, v250
	v_exp_f32_e32 v251, v251
	v_add_f32_e32 v248, 1.0, v248
	v_add_f32_e32 v249, 1.0, v249
	v_add_f32_e32 v250, 1.0, v250
	v_add_f32_e32 v251, 1.0, v251
	v_rcp_f32_e32 v248, v248
	v_rcp_f32_e32 v249, v249
	v_rcp_f32_e32 v250, v250
	v_rcp_f32_e32 v251, v251
	v_mul_f32_e32 v244, v248, v244
	v_mul_f32_e32 v245, v249, v245
	v_mul_f32_e32 v246, v250, v246
	v_mul_f32_e32 v247, v251, v247
	s_waitcnt lgkmcnt(0)
	v_fmac_f32_e32 v91, v84, v85
	v_mul_f32_e32 v248, v91, v244
	v_bfe_u32 v244, v248, 16, 1
	v_add3_u32 v248, v248, v244, s82
	ds_write_b16_d16_hi v173, v248
	v_fmac_f32_e32 v117, v91, v86
	v_mul_f32_e32 v249, v117, v245
	v_bfe_u32 v245, v249, 16, 1
	v_add3_u32 v249, v249, v245, s82
	ds_write_b16_d16_hi v175, v249
	v_fmac_f32_e32 v119, v117, v87
	v_mul_f32_e32 v250, v119, v246
	v_bfe_u32 v246, v250, 16, 1
	v_add3_u32 v250, v250, v246, s82
	ds_write_b16_d16_hi v177, v250
	v_fmac_f32_e32 v243, v119, v90
	v_mul_f32_e32 v251, v243, v247
	v_bfe_u32 v247, v251, 16, 1
	v_add3_u32 v251, v251, v247, s82
	ds_write_b16_d16_hi v179, v251
	s_cmp_lg_u32 s26, 8
	s_waitcnt lgkmcnt(0)
	s_barrier
	ds_read_b128 v[84:87], v145
	s_waitcnt lgkmcnt(0)
	global_store_dwordx4 v[88:89], v[84:87], off
	s_cbranch_scc0 .LBB0_590

.Llru_c1:
	v_add_u32_e32 v85, 0x1e1b0, v180
	ds_read_b32 v86, v85 offset:0
	ds_read_b32 v90, v85 offset:2048
	ds_read_b32 v87, v85 offset:64
	ds_read_b32 v91, v85 offset:2112
	ds_read_b32 v88, v85 offset:128
	ds_read_b32 v117, v85 offset:2176
	ds_read_b32 v89, v85 offset:192
	ds_read_b32 v119, v85 offset:2240
	s_waitcnt lgkmcnt(0)
	ds_read_b32 v243, v85 offset:256
	ds_read_b32 v247, v85 offset:2304
	ds_read_b32 v244, v85 offset:320
	ds_read_b32 v248, v85 offset:2368
	ds_read_b32 v245, v85 offset:384
	ds_read_b32 v249, v85 offset:2432
	ds_read_b32 v246, v85 offset:448
	ds_read_b32 v250, v85 offset:2496
	ds_write_b32 v85, v84 offset:4096
	v_fmac_f32_e32 v90, v84, v86
	ds_write_b32 v85, v90 offset:4160
	v_fmac_f32_e32 v91, v90, v87
	ds_write_b32 v85, v91 offset:4224
	v_fmac_f32_e32 v117, v91, v88
	ds_write_b32 v85, v117 offset:4288
	v_fmac_f32_e32 v119, v117, v89
	v_mov_b32_e32 v84, v119
	s_waitcnt lgkmcnt(0)
	ds_read_b32 v86, v85 offset:512
	ds_read_b32 v90, v85 offset:2560
	ds_read_b32 v87, v85 offset:576
	ds_read_b32 v91, v85 offset:2624
	ds_read_b32 v88, v85 offset:640
	ds_read_b32 v117, v85 offset:2688
	ds_read_b32 v89, v85 offset:704
	ds_read_b32 v119, v85 offset:2752
	ds_write_b32 v85, v84 offset:4352
	v_fmac_f32_e32 v247, v84, v243
	ds_write_b32 v85, v247 offset:4416
	v_fmac_f32_e32 v248, v247, v244
	ds_write_b32 v85, v248 offset:4480
	v_fmac_f32_e32 v249, v248, v245
	ds_write_b32 v85, v249 offset:4544
	v_fmac_f32_e32 v250, v249, v246
	v_mov_b32_e32 v84, v250
	s_waitcnt lgkmcnt(0)
	ds_read_b32 v243, v85 offset:768
	ds_read_b32 v247, v85 offset:2816
	ds_read_b32 v244, v85 offset:832
	ds_read_b32 v248, v85 offset:2880
	ds_read_b32 v245, v85 offset:896
	ds_read_b32 v249, v85 offset:2944
	ds_read_b32 v246, v85 offset:960
	ds_read_b32 v250, v85 offset:3008
	ds_write_b32 v85, v84 offset:4608
	v_fmac_f32_e32 v90, v84, v86
	ds_write_b32 v85, v90 offset:4672
	v_fmac_f32_e32 v91, v90, v87
	ds_write_b32 v85, v91 offset:4736
	v_fmac_f32_e32 v117, v91, v88
	ds_write_b32 v85, v117 offset:4800
	v_fmac_f32_e32 v119, v117, v89
	v_mov_b32_e32 v84, v119
	s_waitcnt lgkmcnt(0)
	ds_read_b32 v86, v85 offset:1024
	ds_read_b32 v90, v85 offset:3072
	ds_read_b32 v87, v85 offset:1088
	ds_read_b32 v91, v85 offset:3136
	ds_read_b32 v88, v85 offset:1152
	ds_read_b32 v117, v85 offset:3200
	ds_read_b32 v89, v85 offset:1216
	ds_read_b32 v119, v85 offset:3264
	ds_write_b32 v85, v84 offset:4864
	v_fmac_f32_e32 v247, v84, v243
	ds_write_b32 v85, v247 offset:4928
	v_fmac_f32_e32 v248, v247, v244
	ds_write_b32 v85, v248 offset:4992
	v_fmac_f32_e32 v249, v248, v245
	ds_write_b32 v85, v249 offset:5056
	v_fmac_f32_e32 v250, v249, v246
	v_mov_b32_e32 v84, v250
	s_waitcnt lgkmcnt(0)
	ds_read_b32 v243, v85 offset:1280
	ds_read_b32 v247, v85 offset:3328
	ds_read_b32 v244, v85 offset:1344
	ds_read_b32 v248, v85 offset:3392
	ds_read_b32 v245, v85 offset:1408
	ds_read_b32 v249, v85 offset:3456
	ds_read_b32 v246, v85 offset:1472
	ds_read_b32 v250, v85 offset:3520
	ds_write_b32 v85, v84 offset:5120
	v_fmac_f32_e32 v90, v84, v86
	ds_write_b32 v85, v90 offset:5184
	v_fmac_f32_e32 v91, v90, v87
	ds_write_b32 v85, v91 offset:5248
	v_fmac_f32_e32 v117, v91, v88
	ds_write_b32 v85, v117 offset:5312
	v_fmac_f32_e32 v119, v117, v89
	v_mov_b32_e32 v84, v119
	s_waitcnt lgkmcnt(0)
	ds_read_b32 v86, v85 offset:1536
	ds_read_b32 v90, v85 offset:3584
	ds_read_b32 v87, v85 offset:1600
	ds_read_b32 v91, v85 offset:3648
	ds_read_b32 v88, v85 offset:1664
	ds_read_b32 v117, v85 offset:3712
	ds_read_b32 v89, v85 offset:1728
	ds_read_b32 v119, v85 offset:3776
	ds_write_b32 v85, v84 offset:5376
	v_fmac_f32_e32 v247, v84, v243
	ds_write_b32 v85, v247 offset:5440
	v_fmac_f32_e32 v248, v247, v244
	ds_write_b32 v85, v248 offset:5504
	v_fmac_f32_e32 v249, v248, v245
	ds_write_b32 v85, v249 offset:5568
	v_fmac_f32_e32 v250, v249, v246
	v_mov_b32_e32 v84, v250
	s_waitcnt lgkmcnt(0)
	ds_read_b32 v243, v85 offset:1792
	ds_read_b32 v247, v85 offset:3840
	ds_read_b32 v244, v85 offset:1856
	ds_read_b32 v248, v85 offset:3904
	ds_read_b32 v245, v85 offset:1920
	ds_read_b32 v249, v85 offset:3968
	ds_read_b32 v246, v85 offset:1984
	ds_read_b32 v250, v85 offset:4032
	ds_write_b32 v85, v84 offset:5632
	v_fmac_f32_e32 v90, v84, v86
	ds_write_b32 v85, v90 offset:5696
	v_fmac_f32_e32 v91, v90, v87
	ds_write_b32 v85, v91 offset:5760
	v_fmac_f32_e32 v117, v91, v88
	ds_write_b32 v85, v117 offset:5824
	v_fmac_f32_e32 v119, v117, v89
	v_mov_b32_e32 v84, v119
	s_waitcnt lgkmcnt(0)
	ds_write_b32 v85, v84 offset:5888
	v_fmac_f32_e32 v247, v84, v243
	ds_write_b32 v85, v247 offset:5952
	v_fmac_f32_e32 v248, v247, v244
	ds_write_b32 v85, v248 offset:6016
	v_fmac_f32_e32 v249, v248, v245
	ds_write_b32 v85, v249 offset:6080
	v_fmac_f32_e32 v250, v249, v246
	v_mov_b32_e32 v84, v250
	ds_write_b32 v143, v84
	s_branch .LBB0_592

.LBB0_880:
	s_or_b64 exec, exec, s[56:57]
	s_add_i32 s6, s21, s62
	s_ashr_i32 s7, s6, 31
	s_lshl_b64 s[8:9], s[6:7], 12
	v_lshl_add_u64 v[20:21], v[118:119], 0, s[8:9]
	s_barrier
	v_mov_b32_e32 v0, s78
	ds_read_b128 v[0:3], v0
	global_load_dwordx4 v[136:139], v[120:121], off
	global_load_dwordx4 v[140:143], v[120:121], off offset:16
	global_load_dwordx4 v[144:147], v[120:121], off offset:2048
	global_load_dwordx4 v[148:151], v[120:121], off offset:2064
	global_load_dwordx4 v[152:155], v[122:123], off
	global_load_dwordx4 v[156:159], v[122:123], off offset:16
	global_load_dwordx4 v[160:163], v[124:125], off
	global_load_dwordx4 v[164:167], v[124:125], off offset:16
	global_load_dwordx4 v[24:27], v[20:21], off
	global_load_dwordx4 v[28:31], v[20:21], off offset:1024
	global_load_dwordx4 v[32:35], v[20:21], off offset:2048
	global_load_dwordx4 v[36:39], v[20:21], off offset:3072
	v_lshl_add_u64 v[176:177], v[126:127], 0, s[8:9]
	s_or_b32 s8, s6, 1
	s_ashr_i32 s9, s8, 31
	s_lshl_b64 s[8:9], s[8:9], 12
	v_lshl_add_u64 v[20:21], v[118:119], 0, s[8:9]
	global_load_dwordx4 v[40:43], v[20:21], off
	global_load_dwordx4 v[44:47], v[20:21], off offset:1024
	global_load_dwordx4 v[48:51], v[20:21], off offset:2048
	global_load_dwordx4 v[52:55], v[20:21], off offset:3072
	s_or_b32 s10, s6, 2
	s_ashr_i32 s11, s10, 31
	s_lshl_b64 s[10:11], s[10:11], 12
	v_lshl_add_u64 v[20:21], v[118:119], 0, s[10:11]
	global_load_dwordx4 v[56:59], v[20:21], off
	global_load_dwordx4 v[60:63], v[20:21], off offset:1024
	global_load_dwordx4 v[64:67], v[20:21], off offset:2048
	global_load_dwordx4 v[68:71], v[20:21], off offset:3072
	s_or_b32 s6, s6, 3
	s_ashr_i32 s7, s6, 31
	s_lshl_b64 s[6:7], s[6:7], 12
	v_lshl_add_u64 v[20:21], v[118:119], 0, s[6:7]
	global_load_dwordx4 v[72:75], v[20:21], off
	global_load_dwordx4 v[76:79], v[20:21], off offset:1024
	global_load_dwordx4 v[168:171], v[20:21], off offset:2048
	global_load_dwordx4 v[172:175], v[20:21], off offset:3072
	s_add_i32 s8, s21, s79
	s_ashr_i32 s9, s8, 31
	s_lshl_b64 s[8:9], s[8:9], 12
	v_lshl_add_u64 v[178:179], v[126:127], 0, s[8:9]
	s_add_i32 s8, s21, s84
	s_ashr_i32 s9, s8, 31
	s_lshl_b64 s[8:9], s[8:9], 12
	v_lshl_add_u64 v[180:181], v[126:127], 0, s[8:9]
	s_add_i32 s8, s21, s91
	s_ashr_i32 s9, s8, 31
	s_lshl_b64 s[8:9], s[8:9], 12
	v_lshl_add_u64 v[182:183], v[126:127], 0, s[8:9]
	s_add_i32 s60, s60, s61
	s_waitcnt vmcnt(0)
	v_lshlrev_b32_e32 v4, 16, v24
	v_and_b32_e32 v5, 0xffff0000, v24
	v_lshlrev_b32_e32 v6, 16, v25
	v_and_b32_e32 v7, 0xffff0000, v25
	v_lshlrev_b32_e32 v8, 16, v26
	v_and_b32_e32 v9, 0xffff0000, v26
	v_lshlrev_b32_e32 v10, 16, v27
	v_and_b32_e32 v11, 0xffff0000, v27
	s_waitcnt lgkmcnt(0)
	v_pk_mul_f32 v[4:5], v[0:1], v[4:5] op_sel_hi:[0,1]
	v_pk_mul_f32 v[6:7], v[0:1], v[6:7] op_sel_hi:[0,1]
	v_pk_mul_f32 v[8:9], v[0:1], v[8:9] op_sel_hi:[0,1]
	v_pk_mul_f32 v[10:11], v[0:1], v[10:11] op_sel_hi:[0,1]
	v_pk_mul_f32 v[4:5], v[136:137], v[4:5]
	v_pk_mul_f32 v[6:7], v[138:139], v[6:7]
	v_pk_mul_f32 v[8:9], v[140:141], v[8:9]
	v_pk_mul_f32 v[10:11], v[142:143], v[10:11]
	v_cvt_pk_bf16_f32 v24, v4, v5
	v_cvt_pk_bf16_f32 v25, v6, v7
	v_cvt_pk_bf16_f32 v26, v8, v9
	v_cvt_pk_bf16_f32 v27, v10, v11
	global_store_dwordx4 v[176:177], v[24:27], off
	v_lshlrev_b32_e32 v12, 16, v28
	v_and_b32_e32 v13, 0xffff0000, v28
	v_lshlrev_b32_e32 v14, 16, v29
	v_and_b32_e32 v15, 0xffff0000, v29
	v_lshlrev_b32_e32 v16, 16, v30
	v_and_b32_e32 v17, 0xffff0000, v30
	v_lshlrev_b32_e32 v18, 16, v31
	v_and_b32_e32 v19, 0xffff0000, v31
	v_pk_mul_f32 v[12:13], v[0:1], v[12:13] op_sel_hi:[0,1]
	v_pk_mul_f32 v[14:15], v[0:1], v[14:15] op_sel_hi:[0,1]
	v_pk_mul_f32 v[16:17], v[0:1], v[16:17] op_sel_hi:[0,1]
	v_pk_mul_f32 v[18:19], v[0:1], v[18:19] op_sel_hi:[0,1]
	v_pk_mul_f32 v[12:13], v[144:145], v[12:13]
	v_pk_mul_f32 v[14:15], v[146:147], v[14:15]
	v_pk_mul_f32 v[16:17], v[148:149], v[16:17]
	v_pk_mul_f32 v[18:19], v[150:151], v[18:19]
	v_cvt_pk_bf16_f32 v28, v12, v13
	v_cvt_pk_bf16_f32 v29, v14, v15
	v_cvt_pk_bf16_f32 v30, v16, v17
	v_cvt_pk_bf16_f32 v31, v18, v19
	global_store_dwordx4 v[176:177], v[28:31], off offset:1024
	v_lshlrev_b32_e32 v4, 16, v32
	v_and_b32_e32 v5, 0xffff0000, v32
	v_lshlrev_b32_e32 v6, 16, v33
	v_and_b32_e32 v7, 0xffff0000, v33
	v_lshlrev_b32_e32 v8, 16, v34
	v_and_b32_e32 v9, 0xffff0000, v34
	v_lshlrev_b32_e32 v10, 16, v35
	v_and_b32_e32 v11, 0xffff0000, v35
	v_pk_mul_f32 v[4:5], v[0:1], v[4:5] op_sel_hi:[0,1]
	v_pk_mul_f32 v[6:7], v[0:1], v[6:7] op_sel_hi:[0,1]
	v_pk_mul_f32 v[8:9], v[0:1], v[8:9] op_sel_hi:[0,1]
	v_pk_mul_f32 v[10:11], v[0:1], v[10:11] op_sel_hi:[0,1]
	v_pk_mul_f32 v[4:5], v[152:153], v[4:5]
	v_pk_mul_f32 v[6:7], v[154:155], v[6:7]
	v_pk_mul_f32 v[8:9], v[156:157], v[8:9]
	v_pk_mul_f32 v[10:11], v[158:159], v[10:11]
	v_cvt_pk_bf16_f32 v32, v4, v5
	v_cvt_pk_bf16_f32 v33, v6, v7
	v_cvt_pk_bf16_f32 v34, v8, v9
	v_cvt_pk_bf16_f32 v35, v10, v11
	global_store_dwordx4 v[176:177], v[32:35], off offset:2048
	v_lshlrev_b32_e32 v12, 16, v36
	v_and_b32_e32 v13, 0xffff0000, v36
	v_lshlrev_b32_e32 v14, 16, v37
	v_and_b32_e32 v15, 0xffff0000, v37
	v_lshlrev_b32_e32 v16, 16, v38
	v_and_b32_e32 v17, 0xffff0000, v38
	v_lshlrev_b32_e32 v18, 16, v39
	v_and_b32_e32 v19, 0xffff0000, v39
	v_pk_mul_f32 v[12:13], v[0:1], v[12:13] op_sel_hi:[0,1]
	v_pk_mul_f32 v[14:15], v[0:1], v[14:15] op_sel_hi:[0,1]
	v_pk_mul_f32 v[16:17], v[0:1], v[16:17] op_sel_hi:[0,1]
	v_pk_mul_f32 v[18:19], v[0:1], v[18:19] op_sel_hi:[0,1]
	v_pk_mul_f32 v[12:13], v[160:161], v[12:13]
	v_pk_mul_f32 v[14:15], v[162:163], v[14:15]
	v_pk_mul_f32 v[16:17], v[164:165], v[16:17]
	v_pk_mul_f32 v[18:19], v[166:167], v[18:19]
	v_cvt_pk_bf16_f32 v36, v12, v13
	v_cvt_pk_bf16_f32 v37, v14, v15
	v_cvt_pk_bf16_f32 v38, v16, v17
	v_cvt_pk_bf16_f32 v39, v18, v19
	global_store_dwordx4 v[176:177], v[36:39], off offset:3072
	v_lshlrev_b32_e32 v4, 16, v40
	v_and_b32_e32 v5, 0xffff0000, v40
	v_lshlrev_b32_e32 v6, 16, v41
	v_and_b32_e32 v7, 0xffff0000, v41
	v_lshlrev_b32_e32 v8, 16, v42
	v_and_b32_e32 v9, 0xffff0000, v42
	v_lshlrev_b32_e32 v10, 16, v43
	v_and_b32_e32 v11, 0xffff0000, v43
	v_pk_mul_f32 v[4:5], v[0:1], v[4:5] op_sel:[1,0]
	v_pk_mul_f32 v[6:7], v[0:1], v[6:7] op_sel:[1,0]
	v_pk_mul_f32 v[8:9], v[0:1], v[8:9] op_sel:[1,0]
	v_pk_mul_f32 v[10:11], v[0:1], v[10:11] op_sel:[1,0]
	v_pk_mul_f32 v[4:5], v[136:137], v[4:5]
	v_pk_mul_f32 v[6:7], v[138:139], v[6:7]
	v_pk_mul_f32 v[8:9], v[140:141], v[8:9]
	v_pk_mul_f32 v[10:11], v[142:143], v[10:11]
	v_cvt_pk_bf16_f32 v40, v4, v5
	v_cvt_pk_bf16_f32 v41, v6, v7
	v_cvt_pk_bf16_f32 v42, v8, v9
	v_cvt_pk_bf16_f32 v43, v10, v11
	global_store_dwordx4 v[178:179], v[40:43], off
	v_lshlrev_b32_e32 v12, 16, v44
	v_and_b32_e32 v13, 0xffff0000, v44
	v_lshlrev_b32_e32 v14, 16, v45
	v_and_b32_e32 v15, 0xffff0000, v45
	v_lshlrev_b32_e32 v16, 16, v46
	v_and_b32_e32 v17, 0xffff0000, v46
	v_lshlrev_b32_e32 v18, 16, v47
	v_and_b32_e32 v19, 0xffff0000, v47
	v_pk_mul_f32 v[12:13], v[0:1], v[12:13] op_sel:[1,0]
	v_pk_mul_f32 v[14:15], v[0:1], v[14:15] op_sel:[1,0]
	v_pk_mul_f32 v[16:17], v[0:1], v[16:17] op_sel:[1,0]
	v_pk_mul_f32 v[18:19], v[0:1], v[18:19] op_sel:[1,0]
	v_pk_mul_f32 v[12:13], v[144:145], v[12:13]
	v_pk_mul_f32 v[14:15], v[146:147], v[14:15]
	v_pk_mul_f32 v[16:17], v[148:149], v[16:17]
	v_pk_mul_f32 v[18:19], v[150:151], v[18:19]
	v_cvt_pk_bf16_f32 v44, v12, v13
	v_cvt_pk_bf16_f32 v45, v14, v15
	v_cvt_pk_bf16_f32 v46, v16, v17
	v_cvt_pk_bf16_f32 v47, v18, v19
	global_store_dwordx4 v[178:179], v[44:47], off offset:1024
	v_lshlrev_b32_e32 v4, 16, v48
	v_and_b32_e32 v5, 0xffff0000, v48
	v_lshlrev_b32_e32 v6, 16, v49
	v_and_b32_e32 v7, 0xffff0000, v49
	v_lshlrev_b32_e32 v8, 16, v50
	v_and_b32_e32 v9, 0xffff0000, v50
	v_lshlrev_b32_e32 v10, 16, v51
	v_and_b32_e32 v11, 0xffff0000, v51
	v_pk_mul_f32 v[4:5], v[0:1], v[4:5] op_sel:[1,0]
	v_pk_mul_f32 v[6:7], v[0:1], v[6:7] op_sel:[1,0]
	v_pk_mul_f32 v[8:9], v[0:1], v[8:9] op_sel:[1,0]
	v_pk_mul_f32 v[10:11], v[0:1], v[10:11] op_sel:[1,0]
	v_pk_mul_f32 v[4:5], v[152:153], v[4:5]
	v_pk_mul_f32 v[6:7], v[154:155], v[6:7]
	v_pk_mul_f32 v[8:9], v[156:157], v[8:9]
	v_pk_mul_f32 v[10:11], v[158:159], v[10:11]
	v_cvt_pk_bf16_f32 v48, v4, v5
	v_cvt_pk_bf16_f32 v49, v6, v7
	v_cvt_pk_bf16_f32 v50, v8, v9
	v_cvt_pk_bf16_f32 v51, v10, v11
	global_store_dwordx4 v[178:179], v[48:51], off offset:2048
	v_lshlrev_b32_e32 v12, 16, v52
	v_and_b32_e32 v13, 0xffff0000, v52
	v_lshlrev_b32_e32 v14, 16, v53
	v_and_b32_e32 v15, 0xffff0000, v53
	v_lshlrev_b32_e32 v16, 16, v54
	v_and_b32_e32 v17, 0xffff0000, v54
	v_lshlrev_b32_e32 v18, 16, v55
	v_and_b32_e32 v19, 0xffff0000, v55
	v_pk_mul_f32 v[12:13], v[0:1], v[12:13] op_sel:[1,0]
	v_pk_mul_f32 v[14:15], v[0:1], v[14:15] op_sel:[1,0]
	v_pk_mul_f32 v[16:17], v[0:1], v[16:17] op_sel:[1,0]
	v_pk_mul_f32 v[18:19], v[0:1], v[18:19] op_sel:[1,0]
	v_pk_mul_f32 v[12:13], v[160:161], v[12:13]
	v_pk_mul_f32 v[14:15], v[162:163], v[14:15]
	v_pk_mul_f32 v[16:17], v[164:165], v[16:17]
	v_pk_mul_f32 v[18:19], v[166:167], v[18:19]
	v_cvt_pk_bf16_f32 v52, v12, v13
	v_cvt_pk_bf16_f32 v53, v14, v15
	v_cvt_pk_bf16_f32 v54, v16, v17
	v_cvt_pk_bf16_f32 v55, v18, v19
	global_store_dwordx4 v[178:179], v[52:55], off offset:3072
	v_lshlrev_b32_e32 v4, 16, v56
	v_and_b32_e32 v5, 0xffff0000, v56
	v_lshlrev_b32_e32 v6, 16, v57
	v_and_b32_e32 v7, 0xffff0000, v57
	v_lshlrev_b32_e32 v8, 16, v58
	v_and_b32_e32 v9, 0xffff0000, v58
	v_lshlrev_b32_e32 v10, 16, v59
	v_and_b32_e32 v11, 0xffff0000, v59
	v_pk_mul_f32 v[4:5], v[2:3], v[4:5] op_sel_hi:[0,1]
	v_pk_mul_f32 v[6:7], v[2:3], v[6:7] op_sel_hi:[0,1]
	v_pk_mul_f32 v[8:9], v[2:3], v[8:9] op_sel_hi:[0,1]
	v_pk_mul_f32 v[10:11], v[2:3], v[10:11] op_sel_hi:[0,1]
	v_pk_mul_f32 v[4:5], v[136:137], v[4:5]
	v_pk_mul_f32 v[6:7], v[138:139], v[6:7]
	v_pk_mul_f32 v[8:9], v[140:141], v[8:9]
	v_pk_mul_f32 v[10:11], v[142:143], v[10:11]
	v_cvt_pk_bf16_f32 v56, v4, v5
	v_cvt_pk_bf16_f32 v57, v6, v7
	v_cvt_pk_bf16_f32 v58, v8, v9
	v_cvt_pk_bf16_f32 v59, v10, v11
	global_store_dwordx4 v[180:181], v[56:59], off
	v_lshlrev_b32_e32 v12, 16, v60
	v_and_b32_e32 v13, 0xffff0000, v60
	v_lshlrev_b32_e32 v14, 16, v61
	v_and_b32_e32 v15, 0xffff0000, v61
	v_lshlrev_b32_e32 v16, 16, v62
	v_and_b32_e32 v17, 0xffff0000, v62
	v_lshlrev_b32_e32 v18, 16, v63
	v_and_b32_e32 v19, 0xffff0000, v63
	v_pk_mul_f32 v[12:13], v[2:3], v[12:13] op_sel_hi:[0,1]
	v_pk_mul_f32 v[14:15], v[2:3], v[14:15] op_sel_hi:[0,1]
	v_pk_mul_f32 v[16:17], v[2:3], v[16:17] op_sel_hi:[0,1]
	v_pk_mul_f32 v[18:19], v[2:3], v[18:19] op_sel_hi:[0,1]
	v_pk_mul_f32 v[12:13], v[144:145], v[12:13]
	v_pk_mul_f32 v[14:15], v[146:147], v[14:15]
	v_pk_mul_f32 v[16:17], v[148:149], v[16:17]
	v_pk_mul_f32 v[18:19], v[150:151], v[18:19]
	v_cvt_pk_bf16_f32 v60, v12, v13
	v_cvt_pk_bf16_f32 v61, v14, v15
	v_cvt_pk_bf16_f32 v62, v16, v17
	v_cvt_pk_bf16_f32 v63, v18, v19
	global_store_dwordx4 v[180:181], v[60:63], off offset:1024
	v_lshlrev_b32_e32 v4, 16, v64
	v_and_b32_e32 v5, 0xffff0000, v64
	v_lshlrev_b32_e32 v6, 16, v65
	v_and_b32_e32 v7, 0xffff0000, v65
	v_lshlrev_b32_e32 v8, 16, v66
	v_and_b32_e32 v9, 0xffff0000, v66
	v_lshlrev_b32_e32 v10, 16, v67
	v_and_b32_e32 v11, 0xffff0000, v67
	v_pk_mul_f32 v[4:5], v[2:3], v[4:5] op_sel_hi:[0,1]
	v_pk_mul_f32 v[6:7], v[2:3], v[6:7] op_sel_hi:[0,1]
	v_pk_mul_f32 v[8:9], v[2:3], v[8:9] op_sel_hi:[0,1]
	v_pk_mul_f32 v[10:11], v[2:3], v[10:11] op_sel_hi:[0,1]
	v_pk_mul_f32 v[4:5], v[152:153], v[4:5]
	v_pk_mul_f32 v[6:7], v[154:155], v[6:7]
	v_pk_mul_f32 v[8:9], v[156:157], v[8:9]
	v_pk_mul_f32 v[10:11], v[158:159], v[10:11]
	v_cvt_pk_bf16_f32 v64, v4, v5
	v_cvt_pk_bf16_f32 v65, v6, v7
	v_cvt_pk_bf16_f32 v66, v8, v9
	v_cvt_pk_bf16_f32 v67, v10, v11
	global_store_dwordx4 v[180:181], v[64:67], off offset:2048
	v_lshlrev_b32_e32 v12, 16, v68
	v_and_b32_e32 v13, 0xffff0000, v68
	v_lshlrev_b32_e32 v14, 16, v69
	v_and_b32_e32 v15, 0xffff0000, v69
	v_lshlrev_b32_e32 v16, 16, v70
	v_and_b32_e32 v17, 0xffff0000, v70
	v_lshlrev_b32_e32 v18, 16, v71
	v_and_b32_e32 v19, 0xffff0000, v71
	v_pk_mul_f32 v[12:13], v[2:3], v[12:13] op_sel_hi:[0,1]
	v_pk_mul_f32 v[14:15], v[2:3], v[14:15] op_sel_hi:[0,1]
	v_pk_mul_f32 v[16:17], v[2:3], v[16:17] op_sel_hi:[0,1]
	v_pk_mul_f32 v[18:19], v[2:3], v[18:19] op_sel_hi:[0,1]
	v_pk_mul_f32 v[12:13], v[160:161], v[12:13]
	v_pk_mul_f32 v[14:15], v[162:163], v[14:15]
	v_pk_mul_f32 v[16:17], v[164:165], v[16:17]
	v_pk_mul_f32 v[18:19], v[166:167], v[18:19]
	v_cvt_pk_bf16_f32 v68, v12, v13
	v_cvt_pk_bf16_f32 v69, v14, v15
	v_cvt_pk_bf16_f32 v70, v16, v17
	v_cvt_pk_bf16_f32 v71, v18, v19
	global_store_dwordx4 v[180:181], v[68:71], off offset:3072
	v_lshlrev_b32_e32 v4, 16, v72
	v_and_b32_e32 v5, 0xffff0000, v72
	v_lshlrev_b32_e32 v6, 16, v73
	v_and_b32_e32 v7, 0xffff0000, v73
	v_lshlrev_b32_e32 v8, 16, v74
	v_and_b32_e32 v9, 0xffff0000, v74
	v_lshlrev_b32_e32 v10, 16, v75
	v_and_b32_e32 v11, 0xffff0000, v75
	v_pk_mul_f32 v[4:5], v[2:3], v[4:5] op_sel:[1,0]
	v_pk_mul_f32 v[6:7], v[2:3], v[6:7] op_sel:[1,0]
	v_pk_mul_f32 v[8:9], v[2:3], v[8:9] op_sel:[1,0]
	v_pk_mul_f32 v[10:11], v[2:3], v[10:11] op_sel:[1,0]
	v_pk_mul_f32 v[4:5], v[136:137], v[4:5]
	v_pk_mul_f32 v[6:7], v[138:139], v[6:7]
	v_pk_mul_f32 v[8:9], v[140:141], v[8:9]
	v_pk_mul_f32 v[10:11], v[142:143], v[10:11]
	v_cvt_pk_bf16_f32 v72, v4, v5
	v_cvt_pk_bf16_f32 v73, v6, v7
	v_cvt_pk_bf16_f32 v74, v8, v9
	v_cvt_pk_bf16_f32 v75, v10, v11
	global_store_dwordx4 v[182:183], v[72:75], off
	v_lshlrev_b32_e32 v12, 16, v76
	v_and_b32_e32 v13, 0xffff0000, v76
	v_lshlrev_b32_e32 v14, 16, v77
	v_and_b32_e32 v15, 0xffff0000, v77
	v_lshlrev_b32_e32 v16, 16, v78
	v_and_b32_e32 v17, 0xffff0000, v78
	v_lshlrev_b32_e32 v18, 16, v79
	v_and_b32_e32 v19, 0xffff0000, v79
	v_pk_mul_f32 v[12:13], v[2:3], v[12:13] op_sel:[1,0]
	v_pk_mul_f32 v[14:15], v[2:3], v[14:15] op_sel:[1,0]
	v_pk_mul_f32 v[16:17], v[2:3], v[16:17] op_sel:[1,0]
	v_pk_mul_f32 v[18:19], v[2:3], v[18:19] op_sel:[1,0]
	v_pk_mul_f32 v[12:13], v[144:145], v[12:13]
	v_pk_mul_f32 v[14:15], v[146:147], v[14:15]
	v_pk_mul_f32 v[16:17], v[148:149], v[16:17]
	v_pk_mul_f32 v[18:19], v[150:151], v[18:19]
	v_cvt_pk_bf16_f32 v76, v12, v13
	v_cvt_pk_bf16_f32 v77, v14, v15
	v_cvt_pk_bf16_f32 v78, v16, v17
	v_cvt_pk_bf16_f32 v79, v18, v19
	global_store_dwordx4 v[182:183], v[76:79], off offset:1024
	v_lshlrev_b32_e32 v4, 16, v168
	v_and_b32_e32 v5, 0xffff0000, v168
	v_lshlrev_b32_e32 v6, 16, v169
	v_and_b32_e32 v7, 0xffff0000, v169
	v_lshlrev_b32_e32 v8, 16, v170
	v_and_b32_e32 v9, 0xffff0000, v170
	v_lshlrev_b32_e32 v10, 16, v171
	v_and_b32_e32 v11, 0xffff0000, v171
	v_pk_mul_f32 v[4:5], v[2:3], v[4:5] op_sel:[1,0]
	v_pk_mul_f32 v[6:7], v[2:3], v[6:7] op_sel:[1,0]
	v_pk_mul_f32 v[8:9], v[2:3], v[8:9] op_sel:[1,0]
	v_pk_mul_f32 v[10:11], v[2:3], v[10:11] op_sel:[1,0]
	v_pk_mul_f32 v[4:5], v[152:153], v[4:5]
	v_pk_mul_f32 v[6:7], v[154:155], v[6:7]
	v_pk_mul_f32 v[8:9], v[156:157], v[8:9]
	v_pk_mul_f32 v[10:11], v[158:159], v[10:11]
	v_cvt_pk_bf16_f32 v168, v4, v5
	v_cvt_pk_bf16_f32 v169, v6, v7
	v_cvt_pk_bf16_f32 v170, v8, v9
	v_cvt_pk_bf16_f32 v171, v10, v11
	global_store_dwordx4 v[182:183], v[168:171], off offset:2048
	v_lshlrev_b32_e32 v12, 16, v172
	v_and_b32_e32 v13, 0xffff0000, v172
	v_lshlrev_b32_e32 v14, 16, v173
	v_and_b32_e32 v15, 0xffff0000, v173
	v_lshlrev_b32_e32 v16, 16, v174
	v_and_b32_e32 v17, 0xffff0000, v174
	v_lshlrev_b32_e32 v18, 16, v175
	v_and_b32_e32 v19, 0xffff0000, v175
	v_pk_mul_f32 v[12:13], v[2:3], v[12:13] op_sel:[1,0]
	v_pk_mul_f32 v[14:15], v[2:3], v[14:15] op_sel:[1,0]
	v_pk_mul_f32 v[16:17], v[2:3], v[16:17] op_sel:[1,0]
	v_pk_mul_f32 v[18:19], v[2:3], v[18:19] op_sel:[1,0]
	v_pk_mul_f32 v[12:13], v[160:161], v[12:13]
	v_pk_mul_f32 v[14:15], v[162:163], v[14:15]
	v_pk_mul_f32 v[16:17], v[164:165], v[16:17]
	v_pk_mul_f32 v[18:19], v[166:167], v[18:19]
	v_cvt_pk_bf16_f32 v172, v12, v13
	v_cvt_pk_bf16_f32 v173, v14, v15
	v_cvt_pk_bf16_f32 v174, v16, v17
	v_cvt_pk_bf16_f32 v175, v18, v19
	global_store_dwordx4 v[182:183], v[172:175], off offset:3072
	s_cmpk_gt_i32 s60, 0xff
	s_barrier
	s_cbranch_scc1 .LBB0_1003
